# grid barrier between out-proj and router replaced by per-row-block arrival counters (partials written through, polled with sc loads)
# speedup vs baseline: 1.0105x; 1.0105x over previous
; __device__ __forceinline__ unsigned cvt_pk_bf16(float lo, float hi) { unsigned r; asm volatile("v_cvt_pk_bf16_f32 %0, %1, %2" : "=v"(r) : "v"(lo), "v"(hi)); return r; }
; __device__ __forceinline__ unsigned pk4_fp8(float a, float b, float c, float d) { int p = 0; p = __builtin_amdgcn_cvt_pk_fp8_f32(a, b, p, false); p = __builtin_amdgcn_cvt_pk_fp8_f32(c, d, p, true); return (unsigned)p; }
;     __device__ __forceinline__ void operator()(AccRef acc, const Unit& u, int wr, int wc, int fr, int fq) const {
;     ...
; #pragma unroll
;         for (int ai = 0; ai < 2; ++ai)
; #pragma unroll
;             for (int m = 0; m < 4; ++m) { const size_t ro = (size_t)(row0 + ai * HALF + m * 16) * DM + col0;
;                 f32x4 xv[2][2];
; #pragma unroll
;                 for (int bj = 0; bj < 2; ++bj)
; #pragma unroll
;                     for (int n = 0; n < 2; ++n) xv[bj][n] = __builtin_nontemporal_load((const f32x4*)(X + ro + bj * HALF + 4 * n));
; #pragma unroll
;                 for (int bj = 0; bj < 2; ++bj) { const f32x4 a = xv[bj][0] + acc[ai][bj][m][0], b = xv[bj][1] + acc[ai][bj][m][1];
;                     { v4u xo; xo.x = cvt_pk_bf16(a[0], a[1]); xo.y = cvt_pk_bf16(a[2], a[3]); xo.z = cvt_pk_bf16(b[0], b[1]); xo.w = cvt_pk_bf16(b[2], b[3]); *(v4u*)(O + ro + bj * HALF) = xo; }
;                     const f32x4 ha = a * gv[bj][0], hb = b * gv[bj][1];
;                     v2u w; w.x = pk4_fp8(ha[0], ha[1], ha[2], ha[3]); w.y = pk4_fp8(hb[0], hb[1], hb[2], hb[3]);
;                     *(v2u*)((unsigned char*)HN + ro + bj * HALF) = w; } }
.LBB0_489:
	v_lshlrev_b32_e32 v241, 1, v254
	v_and_b32_e32 v252, 0x7ff, v254
	v_mbcnt_lo_u32_b32 v243, -1, 0
	v_mbcnt_hi_u32_b32 v243, -1, v243
	v_and_b32_e32 v243, 15, v243
	v_lshl_add_u32 v243, v243, 11, v252
	v_lshlrev_b32_e32 v243, 1, v243
	v_lshlrev_b32_e32 v252, 2, v252
	global_load_dwordx4 v[108:111], v252, s[10:11]
	global_load_dwordx4 v[104:107], v252, s[10:11] offset:16
	global_load_dwordx4 v[100:103], v252, s[10:11] offset:512
	global_load_dwordx4 v[96:99], v252, s[10:11] offset:528
	s_add_u32 s12, s36, 0x40000
	s_addc_u32 s13, s37, 0
	global_load_dwordx4 v[164:167], v240, s[12:13] nt
	global_load_dwordx4 v[168:171], v240, s[12:13] offset:16 nt
	global_load_dwordx4 v[172:175], v240, s[12:13] offset:512 nt
	global_load_dwordx4 v[176:179], v240, s[12:13] offset:528 nt
	s_add_u32 s12, s36, 0x60000
	s_addc_u32 s13, s37, 0
	global_load_dwordx4 v[180:183], v240, s[12:13] nt
	global_load_dwordx4 v[184:187], v240, s[12:13] offset:16 nt
	global_load_dwordx4 v[188:191], v240, s[12:13] offset:512 nt
	global_load_dwordx4 v[192:195], v240, s[12:13] offset:528 nt
	s_add_u32 s12, s36, 0x100000
	s_addc_u32 s13, s37, 0
	global_load_dwordx4 v[196:199], v240, s[12:13] nt
	global_load_dwordx4 v[200:203], v240, s[12:13] offset:16 nt
	global_load_dwordx4 v[204:207], v240, s[12:13] offset:512 nt
	global_load_dwordx4 v[148:151], v240, s[12:13] offset:528 nt
	s_nop 1
	s_waitcnt vmcnt(12)
	v_pk_add_f32 v[140:141], v[140:141], v[208:209]
	v_pk_add_f32 v[142:143], v[142:143], v[210:211]
	v_pk_add_f32 v[136:137], v[136:137], v[212:213]
	v_pk_add_f32 v[138:139], v[138:139], v[214:215]
	v_pk_add_f32 v[132:133], v[132:133], v[216:217]
	v_pk_add_f32 v[134:135], v[134:135], v[218:219]
	v_pk_add_f32 v[128:129], v[128:129], v[220:221]
	v_pk_add_f32 v[130:131], v[130:131], v[222:223]
	s_add_u32 s16, s38, 0x0
	s_addc_u32 s17, s39, 0
	s_add_u32 s20, s60, 0x0
	s_addc_u32 s21, s61, 0
	v_pk_mul_f32 v[208:209], v[108:109], v[140:141]
	v_pk_mul_f32 v[210:211], v[110:111], v[142:143]
	v_pk_mul_f32 v[212:213], v[104:105], v[136:137]
	v_pk_mul_f32 v[214:215], v[106:107], v[138:139]
	v_pk_mul_f32 v[216:217], v[100:101], v[132:133]
	v_pk_mul_f32 v[218:219], v[102:103], v[134:135]
	v_pk_mul_f32 v[220:221], v[96:97], v[128:129]
	v_pk_mul_f32 v[222:223], v[98:99], v[130:131]
	s_nop 0
	v_cvt_pk_bf16_f32 v140, v140, v141
	v_cvt_pk_bf16_f32 v141, v142, v143
	v_cvt_pk_bf16_f32 v142, v136, v137
	v_cvt_pk_bf16_f32 v143, v138, v139
	v_cvt_pk_bf16_f32 v132, v132, v133
	v_cvt_pk_bf16_f32 v133, v134, v135
	v_cvt_pk_bf16_f32 v134, v128, v129
	v_cvt_pk_bf16_f32 v135, v130, v131
	global_store_dwordx4 v241, v[140:143], s[16:17]
	global_store_dwordx4 v241, v[132:135], s[16:17] offset:256
	v_cvt_pk_fp8_f32 v252, v208, v209
	v_cvt_pk_fp8_f32 v253, v212, v213
	v_cvt_pk_fp8_f32 v242, v216, v217
	v_cvt_pk_fp8_f32 v243, v220, v221
	v_cvt_pk_fp8_f32 v252, v210, v211 op_sel:[0,0,1]
	v_cvt_pk_fp8_f32 v253, v214, v215 op_sel:[0,0,1]
	v_cvt_pk_fp8_f32 v242, v218, v219 op_sel:[0,0,1]
	v_cvt_pk_fp8_f32 v243, v222, v223 op_sel:[0,0,1]
	s_nop 0
	global_store_dwordx2 v254, v[252:253], s[20:21]
	global_store_dwordx2 v254, v[242:243], s[20:21] offset:128
	s_nop 1
	s_add_u32 s12, s36, 0x120000
	s_addc_u32 s13, s37, 0
	global_load_dwordx4 v[208:211], v240, s[12:13] nt
	global_load_dwordx4 v[212:215], v240, s[12:13] offset:16 nt
	global_load_dwordx4 v[216:219], v240, s[12:13] offset:512 nt
	global_load_dwordx4 v[220:223], v240, s[12:13] offset:528 nt
	v_pk_add_f32 v[124:125], v[124:125], v[224:225]
	v_pk_add_f32 v[126:127], v[126:127], v[226:227]
	v_pk_add_f32 v[120:121], v[120:121], v[228:229]
	v_pk_add_f32 v[122:123], v[122:123], v[230:231]
	v_pk_add_f32 v[116:117], v[116:117], v[232:233]
	v_pk_add_f32 v[118:119], v[118:119], v[234:235]
	v_pk_add_f32 v[112:113], v[112:113], v[236:237]
	v_pk_add_f32 v[114:115], v[114:115], v[238:239]
	s_add_u32 s16, s38, 0x10000
	s_addc_u32 s17, s39, 0
	s_add_u32 s20, s60, 0x8000
	s_addc_u32 s21, s61, 0
	v_pk_mul_f32 v[224:225], v[108:109], v[124:125]
	v_pk_mul_f32 v[226:227], v[110:111], v[126:127]
	v_pk_mul_f32 v[228:229], v[104:105], v[120:121]
	v_pk_mul_f32 v[230:231], v[106:107], v[122:123]
	v_pk_mul_f32 v[232:233], v[100:101], v[116:117]
	v_pk_mul_f32 v[234:235], v[102:103], v[118:119]
	v_pk_mul_f32 v[236:237], v[96:97], v[112:113]
	v_pk_mul_f32 v[238:239], v[98:99], v[114:115]
	s_nop 0
	v_cvt_pk_bf16_f32 v124, v124, v125
	v_cvt_pk_bf16_f32 v125, v126, v127
	v_cvt_pk_bf16_f32 v126, v120, v121
	v_cvt_pk_bf16_f32 v127, v122, v123
	v_cvt_pk_bf16_f32 v116, v116, v117
	v_cvt_pk_bf16_f32 v117, v118, v119
	v_cvt_pk_bf16_f32 v118, v112, v113
	v_cvt_pk_bf16_f32 v119, v114, v115
	global_store_dwordx4 v241, v[124:127], s[16:17]
	global_store_dwordx4 v241, v[116:119], s[16:17] offset:256
	v_cvt_pk_fp8_f32 v252, v224, v225
	v_cvt_pk_fp8_f32 v253, v228, v229
	v_cvt_pk_fp8_f32 v242, v232, v233
	v_cvt_pk_fp8_f32 v243, v236, v237
	v_cvt_pk_fp8_f32 v252, v226, v227 op_sel:[0,0,1]
	v_cvt_pk_fp8_f32 v253, v230, v231 op_sel:[0,0,1]
	v_cvt_pk_fp8_f32 v242, v234, v235 op_sel:[0,0,1]
	v_cvt_pk_fp8_f32 v243, v238, v239 op_sel:[0,0,1]
	s_nop 0
	global_store_dwordx2 v254, v[252:253], s[20:21]
	global_store_dwordx2 v254, v[242:243], s[20:21] offset:128
	s_nop 1
	s_add_u32 s12, s36, 0x140000
	s_addc_u32 s13, s37, 0
	global_load_dwordx4 v[224:227], v240, s[12:13] nt
	global_load_dwordx4 v[228:231], v240, s[12:13] offset:16 nt
	global_load_dwordx4 v[232:235], v240, s[12:13] offset:512 nt
	global_load_dwordx4 v[236:239], v240, s[12:13] offset:528 nt
	s_waitcnt vmcnt(24)
; __device__ __forceinline__ unsigned cvt_pk_bf16(float lo, float hi) { unsigned r; asm volatile("v_cvt_pk_bf16_f32 %0, %1, %2" : "=v"(r) : "v"(lo), "v"(hi)); return r; }
; __device__ __forceinline__ unsigned pk4_fp8(float a, float b, float c, float d) { int p = 0; p = __builtin_amdgcn_cvt_pk_fp8_f32(a, b, p, false); p = __builtin_amdgcn_cvt_pk_fp8_f32(c, d, p, true); return (unsigned)p; }
;     __device__ __forceinline__ void operator()(AccRef acc, const Unit& u, int wr, int wc, int fr, int fq) const {
;     ...
;             for (int m = 0; m < 4; ++m) { const size_t ro = (size_t)(row0 + ai * HALF + m * 16) * DM + col0;
;                 f32x4 xv[2][2];
; #pragma unroll
;                 for (int bj = 0; bj < 2; ++bj)
; #pragma unroll
;                     for (int n = 0; n < 2; ++n) xv[bj][n] = __builtin_nontemporal_load((const f32x4*)(X + ro + bj * HALF + 4 * n));
; #pragma unroll
;                 for (int bj = 0; bj < 2; ++bj) { const f32x4 a = xv[bj][0] + acc[ai][bj][m][0], b = xv[bj][1] + acc[ai][bj][m][1];
;                     { v4u xo; xo.x = cvt_pk_bf16(a[0], a[1]); xo.y = cvt_pk_bf16(a[2], a[3]); xo.z = cvt_pk_bf16(b[0], b[1]); xo.w = cvt_pk_bf16(b[2], b[3]); *(v4u*)(O + ro + bj * HALF) = xo; }
;                     const f32x4 ha = a * gv[bj][0], hb = b * gv[bj][1];
;                     v2u w; w.x = pk4_fp8(ha[0], ha[1], ha[2], ha[3]); w.y = pk4_fp8(hb[0], hb[1], hb[2], hb[3]);
;                     *(v2u*)((unsigned char*)HN + ro + bj * HALF) = w; } }
; __global__ void __launch_bounds__(512, 2) hymba_fwd(Args args) {
;     ...
;                     for (int s4 = 0; s4 < 4; ++s4) { const int ko = 32 * (4 * hf + s4);
; #pragma unroll
;                         for (int x = 0; x < 2; ++x) xa[x][s4] = *(const v4u*)(xp + (size_t)(16 * x) * DM + ko);
; #pragma unroll
;                         for (int nt = 0; nt < 3; ++nt) { bh[s4][nt] = *(const bf16x8*)(hp + (size_t)(16 * nt) * DM + ko); bl[s4][nt] = *(const bf16x8*)(lp + (size_t)(16 * nt) * DM + ko); } }
	v_pk_add_f32 v[92:93], v[92:93], v[164:165]
	v_pk_add_f32 v[94:95], v[94:95], v[166:167]
	v_pk_add_f32 v[88:89], v[88:89], v[168:169]
	v_pk_add_f32 v[90:91], v[90:91], v[170:171]
	v_pk_add_f32 v[84:85], v[84:85], v[172:173]
	v_pk_add_f32 v[86:87], v[86:87], v[174:175]
	v_pk_add_f32 v[80:81], v[80:81], v[176:177]
	v_pk_add_f32 v[82:83], v[82:83], v[178:179]
	s_add_u32 s16, s38, 0x20000
	s_addc_u32 s17, s39, 0
	s_add_u32 s20, s60, 0x10000
	s_addc_u32 s21, s61, 0
	v_pk_mul_f32 v[164:165], v[108:109], v[92:93]
	v_pk_mul_f32 v[166:167], v[110:111], v[94:95]
	v_pk_mul_f32 v[168:169], v[104:105], v[88:89]
	v_pk_mul_f32 v[170:171], v[106:107], v[90:91]
	v_pk_mul_f32 v[172:173], v[100:101], v[84:85]
	v_pk_mul_f32 v[174:175], v[102:103], v[86:87]
	v_pk_mul_f32 v[176:177], v[96:97], v[80:81]
	v_pk_mul_f32 v[178:179], v[98:99], v[82:83]
	s_nop 0
	v_cvt_pk_bf16_f32 v92, v92, v93
	v_cvt_pk_bf16_f32 v93, v94, v95
	v_cvt_pk_bf16_f32 v94, v88, v89
	v_cvt_pk_bf16_f32 v95, v90, v91
	v_cvt_pk_bf16_f32 v84, v84, v85
	v_cvt_pk_bf16_f32 v85, v86, v87
	v_cvt_pk_bf16_f32 v86, v80, v81
	v_cvt_pk_bf16_f32 v87, v82, v83
	global_store_dwordx4 v241, v[92:95], s[16:17]
	global_store_dwordx4 v241, v[84:87], s[16:17] offset:256
	v_cvt_pk_fp8_f32 v252, v164, v165
	v_cvt_pk_fp8_f32 v253, v168, v169
	v_cvt_pk_fp8_f32 v242, v172, v173
	v_cvt_pk_fp8_f32 v243, v176, v177
	v_cvt_pk_fp8_f32 v252, v166, v167 op_sel:[0,0,1]
	v_cvt_pk_fp8_f32 v253, v170, v171 op_sel:[0,0,1]
	v_cvt_pk_fp8_f32 v242, v174, v175 op_sel:[0,0,1]
	v_cvt_pk_fp8_f32 v243, v178, v179 op_sel:[0,0,1]
	s_nop 0
	global_store_dwordx2 v254, v[252:253], s[20:21]
	global_store_dwordx2 v254, v[242:243], s[20:21] offset:128
	s_nop 1
	s_add_u32 s12, s36, 0x160000
	s_addc_u32 s13, s37, 0
	global_load_dwordx4 v[164:167], v240, s[12:13] nt
	global_load_dwordx4 v[168:171], v240, s[12:13] offset:16 nt
	global_load_dwordx4 v[172:175], v240, s[12:13] offset:512 nt
	global_load_dwordx4 v[176:179], v240, s[12:13] offset:528 nt
	s_waitcnt vmcnt(28)
	v_pk_add_f32 v[76:77], v[76:77], v[180:181]
	v_pk_add_f32 v[78:79], v[78:79], v[182:183]
	v_pk_add_f32 v[72:73], v[72:73], v[184:185]
	v_pk_add_f32 v[74:75], v[74:75], v[186:187]
	v_pk_add_f32 v[68:69], v[68:69], v[188:189]
	v_pk_add_f32 v[70:71], v[70:71], v[190:191]
	v_pk_add_f32 v[64:65], v[64:65], v[192:193]
	v_pk_add_f32 v[66:67], v[66:67], v[194:195]
	s_add_u32 s16, s38, 0x30000
	s_addc_u32 s17, s39, 0
	s_add_u32 s20, s60, 0x18000
	s_addc_u32 s21, s61, 0
	v_pk_mul_f32 v[180:181], v[108:109], v[76:77]
	v_pk_mul_f32 v[182:183], v[110:111], v[78:79]
	v_pk_mul_f32 v[184:185], v[104:105], v[72:73]
	v_pk_mul_f32 v[186:187], v[106:107], v[74:75]
	v_pk_mul_f32 v[188:189], v[100:101], v[68:69]
	v_pk_mul_f32 v[190:191], v[102:103], v[70:71]
	v_pk_mul_f32 v[192:193], v[96:97], v[64:65]
	v_pk_mul_f32 v[194:195], v[98:99], v[66:67]
	s_nop 0
	v_cvt_pk_bf16_f32 v76, v76, v77
	v_cvt_pk_bf16_f32 v77, v78, v79
	v_cvt_pk_bf16_f32 v78, v72, v73
	v_cvt_pk_bf16_f32 v79, v74, v75
	v_cvt_pk_bf16_f32 v68, v68, v69
	v_cvt_pk_bf16_f32 v69, v70, v71
	v_cvt_pk_bf16_f32 v70, v64, v65
	v_cvt_pk_bf16_f32 v71, v66, v67
	global_store_dwordx4 v241, v[76:79], s[16:17]
	global_store_dwordx4 v241, v[68:71], s[16:17] offset:256
	v_cvt_pk_fp8_f32 v252, v180, v181
	v_cvt_pk_fp8_f32 v253, v184, v185
	v_cvt_pk_fp8_f32 v242, v188, v189
	v_cvt_pk_fp8_f32 v243, v192, v193
	v_cvt_pk_fp8_f32 v252, v182, v183 op_sel:[0,0,1]
	v_cvt_pk_fp8_f32 v253, v186, v187 op_sel:[0,0,1]
	v_cvt_pk_fp8_f32 v242, v190, v191 op_sel:[0,0,1]
	v_cvt_pk_fp8_f32 v243, v194, v195 op_sel:[0,0,1]
	s_nop 0
	global_store_dwordx2 v254, v[252:253], s[20:21]
	global_store_dwordx2 v254, v[242:243], s[20:21] offset:128
	v_and_b32_e32 v244, 0x7ff, v254
	v_mbcnt_lo_u32_b32 v243, -1, 0
	v_mbcnt_hi_u32_b32 v243, -1, v243
	v_and_b32_e32 v243, 15, v243
	v_lshl_add_u32 v243, v243, 11, v244
	v_lshlrev_b32_e32 v243, 1, v243
	s_nop 1
	s_add_u32 s12, s26, 0x350000
	s_addc_u32 s13, s27, 0
	global_load_dwordx4 v[180:183], v243, s[12:13]
	s_add_u32 s12, s26, 0x320000
	s_addc_u32 s13, s27, 0
	global_load_dwordx4 v[184:187], v243, s[12:13]
	s_add_u32 s12, s26, 0x360000
	s_addc_u32 s13, s27, 0
	global_load_dwordx4 v[188:191], v243, s[12:13]
	s_add_u32 s12, s26, 0x330000
	s_addc_u32 s13, s27, 0
	global_load_dwordx4 v[192:195], v243, s[12:13]
	s_waitcnt vmcnt(32)
	v_pk_add_f32 v[60:61], v[60:61], v[196:197]
	v_pk_add_f32 v[62:63], v[62:63], v[198:199]
	v_pk_add_f32 v[56:57], v[56:57], v[200:201]
	v_pk_add_f32 v[58:59], v[58:59], v[202:203]
	v_pk_add_f32 v[52:53], v[52:53], v[204:205]
	v_pk_add_f32 v[54:55], v[54:55], v[206:207]
	v_pk_add_f32 v[48:49], v[48:49], v[148:149]
	v_pk_add_f32 v[50:51], v[50:51], v[150:151]
	s_add_u32 s16, s38, 0x80000
	s_addc_u32 s17, s39, 0
	s_add_u32 s20, s60, 0x40000
	s_addc_u32 s21, s61, 0
	v_pk_mul_f32 v[196:197], v[108:109], v[60:61]
	v_pk_mul_f32 v[198:199], v[110:111], v[62:63]
	v_pk_mul_f32 v[200:201], v[104:105], v[56:57]
	v_pk_mul_f32 v[202:203], v[106:107], v[58:59]
	v_pk_mul_f32 v[204:205], v[100:101], v[52:53]
	v_pk_mul_f32 v[206:207], v[102:103], v[54:55]
	v_pk_mul_f32 v[148:149], v[96:97], v[48:49]
	v_pk_mul_f32 v[150:151], v[98:99], v[50:51]
	s_nop 0
	v_cvt_pk_bf16_f32 v60, v60, v61
	v_cvt_pk_bf16_f32 v61, v62, v63
	v_cvt_pk_bf16_f32 v62, v56, v57
	v_cvt_pk_bf16_f32 v63, v58, v59
	v_cvt_pk_bf16_f32 v52, v52, v53
	v_cvt_pk_bf16_f32 v53, v54, v55
	v_cvt_pk_bf16_f32 v54, v48, v49
	v_cvt_pk_bf16_f32 v55, v50, v51
	global_store_dwordx4 v241, v[60:63], s[16:17]
	global_store_dwordx4 v241, v[52:55], s[16:17] offset:256
	v_cvt_pk_fp8_f32 v252, v196, v197
	v_cvt_pk_fp8_f32 v253, v200, v201
	v_cvt_pk_fp8_f32 v242, v204, v205
	v_cvt_pk_fp8_f32 v243, v148, v149
	v_cvt_pk_fp8_f32 v252, v198, v199 op_sel:[0,0,1]
	v_cvt_pk_fp8_f32 v253, v202, v203 op_sel:[0,0,1]
	v_cvt_pk_fp8_f32 v242, v206, v207 op_sel:[0,0,1]
	v_cvt_pk_fp8_f32 v243, v150, v151 op_sel:[0,0,1]
	s_nop 0
	global_store_dwordx2 v254, v[252:253], s[20:21]
	global_store_dwordx2 v254, v[242:243], s[20:21] offset:128
	v_and_b32_e32 v244, 0x7ff, v254
	v_mbcnt_lo_u32_b32 v243, -1, 0
	v_mbcnt_hi_u32_b32 v243, -1, v243
	v_and_b32_e32 v243, 15, v243
	v_lshl_add_u32 v243, v243, 11, v244
	v_lshlrev_b32_e32 v243, 1, v243
	s_nop 1
	s_add_u32 s12, s26, 0x370000
	s_addc_u32 s13, s27, 0
	global_load_dwordx4 v[196:199], v243, s[12:13]
	s_add_u32 s12, s26, 0x340000
	s_addc_u32 s13, s27, 0
	global_load_dwordx4 v[200:203], v243, s[12:13]
	s_add_u32 s12, s26, 0x350100
	s_addc_u32 s13, s27, 0
	global_load_dwordx4 v[204:207], v243, s[12:13]
	s_add_u32 s12, s26, 0x320100
	s_addc_u32 s13, s27, 0
	global_load_dwordx4 v[148:151], v243, s[12:13]
	s_waitcnt vmcnt(32)
; __device__ __forceinline__ unsigned cvt_pk_bf16(float lo, float hi) { unsigned r; asm volatile("v_cvt_pk_bf16_f32 %0, %1, %2" : "=v"(r) : "v"(lo), "v"(hi)); return r; }
; __device__ __forceinline__ unsigned pk4_fp8(float a, float b, float c, float d) { int p = 0; p = __builtin_amdgcn_cvt_pk_fp8_f32(a, b, p, false); p = __builtin_amdgcn_cvt_pk_fp8_f32(c, d, p, true); return (unsigned)p; }
;     __device__ __forceinline__ void operator()(AccRef acc, const Unit& u, int wr, int wc, int fr, int fq) const {
;     ...
;             for (int m = 0; m < 4; ++m) { const size_t ro = (size_t)(row0 + ai * HALF + m * 16) * DM + col0;
;                 f32x4 xv[2][2];
; #pragma unroll
;                 for (int bj = 0; bj < 2; ++bj)
; #pragma unroll
;                     for (int n = 0; n < 2; ++n) xv[bj][n] = __builtin_nontemporal_load((const f32x4*)(X + ro + bj * HALF + 4 * n));
; #pragma unroll
;                 for (int bj = 0; bj < 2; ++bj) { const f32x4 a = xv[bj][0] + acc[ai][bj][m][0], b = xv[bj][1] + acc[ai][bj][m][1];
;                     { v4u xo; xo.x = cvt_pk_bf16(a[0], a[1]); xo.y = cvt_pk_bf16(a[2], a[3]); xo.z = cvt_pk_bf16(b[0], b[1]); xo.w = cvt_pk_bf16(b[2], b[3]); *(v4u*)(O + ro + bj * HALF) = xo; }
;                     const f32x4 ha = a * gv[bj][0], hb = b * gv[bj][1];
;                     v2u w; w.x = pk4_fp8(ha[0], ha[1], ha[2], ha[3]); w.y = pk4_fp8(hb[0], hb[1], hb[2], hb[3]);
;                     *(v2u*)((unsigned char*)HN + ro + bj * HALF) = w; } }
; __global__ void __launch_bounds__(512, 2) hymba_fwd(Args args) {
;     ...
; #pragma unroll
;                 for (int x = 0; x < 2; ++x) {
; #pragma unroll
;                     for (int nt = 0; nt < 3; ++nt)
; #pragma unroll
;                         for (int e = 0; e < 4; ++e) part[(wave * 32 + 16 * x + 4 * kg + e) * 48 + 16 * nt + li] = acc[x][nt][e];
;                     float s1 = ss[x]; s1 += __shfl_xor(s1, 16); s1 += __shfl_xor(s1, 32);
;                     if (kg == 0) ssp[wave * 32 + 16 * x + li] = s1; }
	v_pk_add_f32 v[44:45], v[44:45], v[208:209]
	v_pk_add_f32 v[46:47], v[46:47], v[210:211]
	v_pk_add_f32 v[40:41], v[40:41], v[212:213]
	v_pk_add_f32 v[42:43], v[42:43], v[214:215]
	v_pk_add_f32 v[36:37], v[36:37], v[216:217]
	v_pk_add_f32 v[38:39], v[38:39], v[218:219]
	v_pk_add_f32 v[32:33], v[32:33], v[220:221]
	v_pk_add_f32 v[34:35], v[34:35], v[222:223]
	s_add_u32 s16, s38, 0x90000
	s_addc_u32 s17, s39, 0
	s_add_u32 s20, s60, 0x48000
	s_addc_u32 s21, s61, 0
	v_pk_mul_f32 v[208:209], v[108:109], v[44:45]
	v_pk_mul_f32 v[210:211], v[110:111], v[46:47]
	v_pk_mul_f32 v[212:213], v[104:105], v[40:41]
	v_pk_mul_f32 v[214:215], v[106:107], v[42:43]
	v_pk_mul_f32 v[216:217], v[100:101], v[36:37]
	v_pk_mul_f32 v[218:219], v[102:103], v[38:39]
	v_pk_mul_f32 v[220:221], v[96:97], v[32:33]
	v_pk_mul_f32 v[222:223], v[98:99], v[34:35]
	s_nop 0
	v_cvt_pk_bf16_f32 v44, v44, v45
	v_cvt_pk_bf16_f32 v45, v46, v47
	v_cvt_pk_bf16_f32 v46, v40, v41
	v_cvt_pk_bf16_f32 v47, v42, v43
	v_cvt_pk_bf16_f32 v36, v36, v37
	v_cvt_pk_bf16_f32 v37, v38, v39
	v_cvt_pk_bf16_f32 v38, v32, v33
	v_cvt_pk_bf16_f32 v39, v34, v35
	global_store_dwordx4 v241, v[44:47], s[16:17]
	global_store_dwordx4 v241, v[36:39], s[16:17] offset:256
	v_cvt_pk_fp8_f32 v252, v208, v209
	v_cvt_pk_fp8_f32 v253, v212, v213
	v_cvt_pk_fp8_f32 v242, v216, v217
	v_cvt_pk_fp8_f32 v243, v220, v221
	v_cvt_pk_fp8_f32 v252, v210, v211 op_sel:[0,0,1]
	v_cvt_pk_fp8_f32 v253, v214, v215 op_sel:[0,0,1]
	v_cvt_pk_fp8_f32 v242, v218, v219 op_sel:[0,0,1]
	v_cvt_pk_fp8_f32 v243, v222, v223 op_sel:[0,0,1]
	s_nop 0
	global_store_dwordx2 v254, v[252:253], s[20:21]
	global_store_dwordx2 v254, v[242:243], s[20:21] offset:128
	v_and_b32_e32 v244, 0x7ff, v254
	v_mbcnt_lo_u32_b32 v243, -1, 0
	v_mbcnt_hi_u32_b32 v243, -1, v243
	v_and_b32_e32 v243, 15, v243
	v_lshl_add_u32 v243, v243, 11, v244
	v_lshlrev_b32_e32 v243, 1, v243
	s_nop 1
	s_add_u32 s12, s26, 0x360100
	s_addc_u32 s13, s27, 0
	global_load_dwordx4 v[208:211], v243, s[12:13]
	s_add_u32 s12, s26, 0x330100
	s_addc_u32 s13, s27, 0
	global_load_dwordx4 v[212:215], v243, s[12:13]
	s_add_u32 s12, s26, 0x370100
	s_addc_u32 s13, s27, 0
	global_load_dwordx4 v[216:219], v243, s[12:13]
	s_add_u32 s12, s26, 0x340100
	s_addc_u32 s13, s27, 0
	global_load_dwordx4 v[220:223], v243, s[12:13]
	s_waitcnt vmcnt(32)
	v_pk_add_f32 v[20:21], v[20:21], v[224:225]
	v_pk_add_f32 v[22:23], v[22:23], v[226:227]
	v_pk_add_f32 v[16:17], v[16:17], v[228:229]
	v_pk_add_f32 v[18:19], v[18:19], v[230:231]
	v_pk_add_f32 v[24:25], v[24:25], v[232:233]
	v_pk_add_f32 v[26:27], v[26:27], v[234:235]
	v_pk_add_f32 v[28:29], v[28:29], v[236:237]
	v_pk_add_f32 v[30:31], v[30:31], v[238:239]
	s_add_u32 s16, s38, 0xa0000
	s_addc_u32 s17, s39, 0
	s_add_u32 s20, s60, 0x50000
	s_addc_u32 s21, s61, 0
	v_pk_mul_f32 v[224:225], v[108:109], v[20:21]
	v_pk_mul_f32 v[226:227], v[110:111], v[22:23]
	v_pk_mul_f32 v[228:229], v[104:105], v[16:17]
	v_pk_mul_f32 v[230:231], v[106:107], v[18:19]
	v_pk_mul_f32 v[232:233], v[100:101], v[24:25]
	v_pk_mul_f32 v[234:235], v[102:103], v[26:27]
	v_pk_mul_f32 v[236:237], v[96:97], v[28:29]
	v_pk_mul_f32 v[238:239], v[98:99], v[30:31]
	s_nop 0
	v_cvt_pk_bf16_f32 v20, v20, v21
	v_cvt_pk_bf16_f32 v21, v22, v23
	v_cvt_pk_bf16_f32 v22, v16, v17
	v_cvt_pk_bf16_f32 v23, v18, v19
	v_cvt_pk_bf16_f32 v24, v24, v25
	v_cvt_pk_bf16_f32 v25, v26, v27
	v_cvt_pk_bf16_f32 v26, v28, v29
	v_cvt_pk_bf16_f32 v27, v30, v31
	global_store_dwordx4 v241, v[20:23], s[16:17]
	global_store_dwordx4 v241, v[24:27], s[16:17] offset:256
	v_cvt_pk_fp8_f32 v252, v224, v225
	v_cvt_pk_fp8_f32 v253, v228, v229
	v_cvt_pk_fp8_f32 v242, v232, v233
	v_cvt_pk_fp8_f32 v243, v236, v237
	v_cvt_pk_fp8_f32 v252, v226, v227 op_sel:[0,0,1]
	v_cvt_pk_fp8_f32 v253, v230, v231 op_sel:[0,0,1]
	v_cvt_pk_fp8_f32 v242, v234, v235 op_sel:[0,0,1]
	v_cvt_pk_fp8_f32 v243, v238, v239 op_sel:[0,0,1]
	s_nop 0
	global_store_dwordx2 v254, v[252:253], s[20:21]
	global_store_dwordx2 v254, v[242:243], s[20:21] offset:128
	s_waitcnt vmcnt(28)
	v_pk_add_f32 v[4:5], v[4:5], v[164:165]
	v_pk_add_f32 v[6:7], v[6:7], v[166:167]
	v_pk_add_f32 v[0:1], v[0:1], v[168:169]
	v_pk_add_f32 v[2:3], v[2:3], v[170:171]
	v_pk_add_f32 v[8:9], v[8:9], v[172:173]
	v_pk_add_f32 v[10:11], v[10:11], v[174:175]
	v_pk_add_f32 v[12:13], v[12:13], v[176:177]
	v_pk_add_f32 v[14:15], v[14:15], v[178:179]
	s_add_u32 s16, s38, 0xb0000
	s_addc_u32 s17, s39, 0
	s_add_u32 s20, s60, 0x58000
	s_addc_u32 s21, s61, 0
	v_pk_mul_f32 v[164:165], v[108:109], v[4:5]
	v_pk_mul_f32 v[166:167], v[110:111], v[6:7]
	v_pk_mul_f32 v[168:169], v[104:105], v[0:1]
	v_pk_mul_f32 v[170:171], v[106:107], v[2:3]
	v_pk_mul_f32 v[172:173], v[100:101], v[8:9]
	v_pk_mul_f32 v[174:175], v[102:103], v[10:11]
	v_pk_mul_f32 v[176:177], v[96:97], v[12:13]
	v_pk_mul_f32 v[178:179], v[98:99], v[14:15]
	s_nop 0
	v_cvt_pk_bf16_f32 v4, v4, v5
	v_cvt_pk_bf16_f32 v5, v6, v7
	v_cvt_pk_bf16_f32 v6, v0, v1
	v_cvt_pk_bf16_f32 v7, v2, v3
	v_cvt_pk_bf16_f32 v8, v8, v9
	v_cvt_pk_bf16_f32 v9, v10, v11
	v_cvt_pk_bf16_f32 v10, v12, v13
	v_cvt_pk_bf16_f32 v11, v14, v15
	global_store_dwordx4 v241, v[4:7], s[16:17]
	global_store_dwordx4 v241, v[8:11], s[16:17] offset:256
	v_cvt_pk_fp8_f32 v252, v164, v165
	v_cvt_pk_fp8_f32 v253, v168, v169
	v_cvt_pk_fp8_f32 v242, v172, v173
	v_cvt_pk_fp8_f32 v243, v176, v177
	v_cvt_pk_fp8_f32 v252, v166, v167 op_sel:[0,0,1]
	v_cvt_pk_fp8_f32 v253, v170, v171 op_sel:[0,0,1]
	v_cvt_pk_fp8_f32 v242, v174, v175 op_sel:[0,0,1]
	v_cvt_pk_fp8_f32 v243, v178, v179 op_sel:[0,0,1]
	s_nop 0
	global_store_dwordx2 v254, v[252:253], s[20:21]
	global_store_dwordx2 v254, v[242:243], s[20:21] offset:128
	v_mbcnt_lo_u32_b32 v164, -1, 0
	v_mbcnt_hi_u32_b32 v164, -1, v164
	v_and_b32_e32 v165, 15, v164
	v_lshrrev_b32_e32 v166, 4, v164
	s_lshr_b32 s33, s77, 6
	s_lshr_b32 s41, s78, 5
	s_lshl_b32 s100, s33, 2
	s_add_i32 s100, s100, s41
	v_lshl_add_u32 v167, v166, 2, s77
	v_mul_u32_u24_e32 v167, 48, v167
	v_add_u32_e32 v167, v167, v165
	v_lshlrev_b32_e32 v167, 2, v167
	v_add_u32_e32 v168, s77, v165
	v_lshlrev_b32_e32 v168, 2, v168
	v_lshlrev_b32_e32 v169, 2, v166
	v_sub_u32_e32 v169, v165, v169
	v_cmp_eq_u32_e64 s[12:13], 0, v169
	v_cmp_eq_u32_e64 s[16:17], 1, v169
	v_cmp_eq_u32_e64 s[20:21], 2, v169
	v_cmp_eq_u32_e64 s[22:23], 3, v169
	s_barrier
; __global__ void __launch_bounds__(512, 2) hymba_fwd(Args args) {
;     ...
;                     for (int s4 = 0; s4 < 4; ++s4)
; #pragma unroll
;                         for (int x = 0; x < 2; ++x) { const v4u q = xa[x][s4];
;                             ss[x] += (bf_lo(q.x) * bf_lo(q.x) + bf_hi(q.x) * bf_hi(q.x)) + (bf_lo(q.y) * bf_lo(q.y) + bf_hi(q.y) * bf_hi(q.y)) + (bf_lo(q.z) * bf_lo(q.z) + bf_hi(q.z) * bf_hi(q.z)) + (bf_lo(q.w) * bf_lo(q.w) + bf_hi(q.w) * bf_hi(q.w)); }
;                     __builtin_amdgcn_sched_barrier(0);
; #pragma unroll
;                     for (int s4 = 0; s4 < 4; ++s4)
; #pragma unroll
;                         for (int x = 0; x < 2; ++x) { const bf16x8 xh = __builtin_bit_cast(bf16x8, xa[x][s4]);
; #pragma unroll
;                             for (int nt = 0; nt < 3; ++nt) {
;                                 acc[x][nt] = __builtin_amdgcn_mfma_f32_16x16x32_bf16(xh, bl[s4][nt], acc[x][nt], 0, 0, 0);
;                                 acc[x][nt] = __builtin_amdgcn_mfma_f32_16x16x32_bf16(xh, bh[s4][nt], acc[x][nt], 0, 0, 0); } }
;                 }
; #pragma unroll
;                 for (int x = 0; x < 2; ++x) {
; #pragma unroll
;                     for (int nt = 0; nt < 3; ++nt)
; #pragma unroll
;                         for (int e = 0; e < 4; ++e) part[(wave * 32 + 16 * x + 4 * kg + e) * 48 + 16 * nt + li] = acc[x][nt][e];
;                     float s1 = ss[x]; s1 += __shfl_xor(s1, 16); s1 += __shfl_xor(s1, 32);
;                     if (kg == 0) ssp[wave * 32 + 16 * x + li] = s1; }
	v_mov_b32_e32 v172, 0
	v_mov_b32_e32 v173, 0
	v_mov_b32_e32 v174, 0
	v_mov_b32_e32 v175, 0
	s_mul_i32 s101, s100, 0x1800
	v_lshl_add_u32 v170, v164, 4, s101
	ds_write_b128 v170, v[172:175] offset:0
	ds_write_b128 v170, v[172:175] offset:1024
	ds_write_b128 v170, v[172:175] offset:2048
	ds_write_b128 v170, v[172:175] offset:3072
	ds_write_b128 v170, v[172:175] offset:4096
	ds_write_b128 v170, v[172:175] offset:5120
	s_lshl_b32 s101, s100, 7
	v_lshl_add_u32 v171, v164, 2, s101
	s_mov_b32 exec_lo, -1
	s_mov_b32 exec_hi, 0
	ds_write_b32 v171, v172 offset:49152
	s_mov_b64 exec, -1
	s_waitcnt vmcnt(8) lgkmcnt(0)
	s_barrier
	v_mov_b32_e32 v176, 0x4b800000
	v_mov_b32_e32 v177, 0x47800000
	v_mfma_f32_16x16x32_bf16 v[224:227], v[140:143], v[180:183], 0
	v_mfma_f32_16x16x32_bf16 v[224:227], v[140:143], v[184:187], v[224:227]
	v_mfma_f32_16x16x32_bf16 v[224:227], v[132:135], v[204:207], v[224:227]
	v_mfma_f32_16x16x32_bf16 v[224:227], v[132:135], v[148:151], v[224:227]
	v_mfma_f32_16x16x32_bf16 v[228:231], v[140:143], v[188:191], 0
	v_mfma_f32_16x16x32_bf16 v[228:231], v[140:143], v[192:195], v[228:231]
	v_mfma_f32_16x16x32_bf16 v[228:231], v[132:135], v[208:211], v[228:231]
	v_mfma_f32_16x16x32_bf16 v[228:231], v[132:135], v[212:215], v[228:231]
	v_mfma_f32_16x16x32_bf16 v[232:235], v[140:143], v[196:199], 0
	v_mfma_f32_16x16x32_bf16 v[232:235], v[140:143], v[200:203], v[232:235]
	v_mfma_f32_16x16x32_bf16 v[232:235], v[132:135], v[216:219], v[232:235]
	v_mfma_f32_16x16x32_bf16 v[232:235], v[132:135], v[220:223], v[232:235]
	v_mfma_f32_16x16x32_bf16 v[236:239], v[140:143], v[140:143], 0
	v_mfma_f32_16x16x32_bf16 v[236:239], v[132:135], v[132:135], v[236:239]
	s_nop 7
	s_nop 3
	v_mul_f32_e32 v224, v224, v176
	v_cvt_i32_f32_e32 v224, v224
	v_mul_f32_e32 v225, v225, v176
	v_cvt_i32_f32_e32 v225, v225
	v_mul_f32_e32 v226, v226, v176
	v_cvt_i32_f32_e32 v226, v226
	v_mul_f32_e32 v227, v227, v176
	v_cvt_i32_f32_e32 v227, v227
	v_mul_f32_e32 v228, v228, v176
	v_cvt_i32_f32_e32 v228, v228
	v_mul_f32_e32 v229, v229, v176
	v_cvt_i32_f32_e32 v229, v229
	v_mul_f32_e32 v230, v230, v176
	v_cvt_i32_f32_e32 v230, v230
	v_mul_f32_e32 v231, v231, v176
	v_cvt_i32_f32_e32 v231, v231
	v_mul_f32_e32 v232, v232, v176
	v_cvt_i32_f32_e32 v232, v232
	v_mul_f32_e32 v233, v233, v176
	v_cvt_i32_f32_e32 v233, v233
	v_mul_f32_e32 v234, v234, v176
	v_cvt_i32_f32_e32 v234, v234
	v_mul_f32_e32 v235, v235, v176
	v_cvt_i32_f32_e32 v235, v235
	v_mul_f32_e32 v236, v236, v177
	v_cvt_i32_f32_e32 v236, v236
	v_mul_f32_e32 v237, v237, v177
	v_cvt_i32_f32_e32 v237, v237
	v_mul_f32_e32 v238, v238, v177
	v_cvt_i32_f32_e32 v238, v238
	v_mul_f32_e32 v239, v239, v177
	v_cvt_i32_f32_e32 v239, v239
	ds_add_u32 v167, v224 offset:0
	ds_add_u32 v167, v225 offset:192
	ds_add_u32 v167, v226 offset:384
	ds_add_u32 v167, v227 offset:576
	ds_add_u32 v167, v228 offset:64
	ds_add_u32 v167, v229 offset:256
	ds_add_u32 v167, v230 offset:448
	ds_add_u32 v167, v231 offset:640
	ds_add_u32 v167, v232 offset:128
	ds_add_u32 v167, v233 offset:320
	ds_add_u32 v167, v234 offset:512
	ds_add_u32 v167, v235 offset:704
	s_mov_b64 exec, s[12:13]
	ds_add_u32 v168, v236 offset:49152
	s_mov_b64 exec, s[16:17]
	ds_add_u32 v168, v237 offset:49152
	s_mov_b64 exec, s[20:21]
	ds_add_u32 v168, v238 offset:49152
	s_mov_b64 exec, s[22:23]
	ds_add_u32 v168, v239 offset:49152
	s_mov_b64 exec, -1
	v_mfma_f32_16x16x32_bf16 v[224:227], v[124:127], v[180:183], 0
	v_mfma_f32_16x16x32_bf16 v[224:227], v[124:127], v[184:187], v[224:227]
	v_mfma_f32_16x16x32_bf16 v[224:227], v[116:119], v[204:207], v[224:227]
	v_mfma_f32_16x16x32_bf16 v[224:227], v[116:119], v[148:151], v[224:227]
	v_mfma_f32_16x16x32_bf16 v[228:231], v[124:127], v[188:191], 0
	v_mfma_f32_16x16x32_bf16 v[228:231], v[124:127], v[192:195], v[228:231]
	v_mfma_f32_16x16x32_bf16 v[228:231], v[116:119], v[208:211], v[228:231]
	v_mfma_f32_16x16x32_bf16 v[228:231], v[116:119], v[212:215], v[228:231]
	v_mfma_f32_16x16x32_bf16 v[232:235], v[124:127], v[196:199], 0
	v_mfma_f32_16x16x32_bf16 v[232:235], v[124:127], v[200:203], v[232:235]
	v_mfma_f32_16x16x32_bf16 v[232:235], v[116:119], v[216:219], v[232:235]
	v_mfma_f32_16x16x32_bf16 v[232:235], v[116:119], v[220:223], v[232:235]
	v_mfma_f32_16x16x32_bf16 v[236:239], v[124:127], v[124:127], 0
	v_mfma_f32_16x16x32_bf16 v[236:239], v[116:119], v[116:119], v[236:239]
	s_nop 7
	s_nop 3
	v_mul_f32_e32 v224, v224, v176
	v_cvt_i32_f32_e32 v224, v224
	v_mul_f32_e32 v225, v225, v176
	v_cvt_i32_f32_e32 v225, v225
	v_mul_f32_e32 v226, v226, v176
	v_cvt_i32_f32_e32 v226, v226
	v_mul_f32_e32 v227, v227, v176
	v_cvt_i32_f32_e32 v227, v227
	v_mul_f32_e32 v228, v228, v176
	v_cvt_i32_f32_e32 v228, v228
	v_mul_f32_e32 v229, v229, v176
	v_cvt_i32_f32_e32 v229, v229
	v_mul_f32_e32 v230, v230, v176
	v_cvt_i32_f32_e32 v230, v230
	v_mul_f32_e32 v231, v231, v176
	v_cvt_i32_f32_e32 v231, v231
	v_mul_f32_e32 v232, v232, v176
	v_cvt_i32_f32_e32 v232, v232
	v_mul_f32_e32 v233, v233, v176
	v_cvt_i32_f32_e32 v233, v233
	v_mul_f32_e32 v234, v234, v176
	v_cvt_i32_f32_e32 v234, v234
	v_mul_f32_e32 v235, v235, v176
	v_cvt_i32_f32_e32 v235, v235
	v_mul_f32_e32 v236, v236, v177
	v_cvt_i32_f32_e32 v236, v236
	v_mul_f32_e32 v237, v237, v177
	v_cvt_i32_f32_e32 v237, v237
	v_mul_f32_e32 v238, v238, v177
	v_cvt_i32_f32_e32 v238, v238
	v_mul_f32_e32 v239, v239, v177
	v_cvt_i32_f32_e32 v239, v239
	ds_add_u32 v167, v224 offset:3072
	ds_add_u32 v167, v225 offset:3264
	ds_add_u32 v167, v226 offset:3456
	ds_add_u32 v167, v227 offset:3648
	ds_add_u32 v167, v228 offset:3136
	ds_add_u32 v167, v229 offset:3328
	ds_add_u32 v167, v230 offset:3520
	ds_add_u32 v167, v231 offset:3712
; __global__ void __launch_bounds__(512, 2) hymba_fwd(Args args) {
;     ...
;                     for (int s4 = 0; s4 < 4; ++s4)
; #pragma unroll
;                         for (int x = 0; x < 2; ++x) { const v4u q = xa[x][s4];
;                             ss[x] += (bf_lo(q.x) * bf_lo(q.x) + bf_hi(q.x) * bf_hi(q.x)) + (bf_lo(q.y) * bf_lo(q.y) + bf_hi(q.y) * bf_hi(q.y)) + (bf_lo(q.z) * bf_lo(q.z) + bf_hi(q.z) * bf_hi(q.z)) + (bf_lo(q.w) * bf_lo(q.w) + bf_hi(q.w) * bf_hi(q.w)); }
;                     __builtin_amdgcn_sched_barrier(0);
; #pragma unroll
;                     for (int s4 = 0; s4 < 4; ++s4)
; #pragma unroll
;                         for (int x = 0; x < 2; ++x) { const bf16x8 xh = __builtin_bit_cast(bf16x8, xa[x][s4]);
; #pragma unroll
;                             for (int nt = 0; nt < 3; ++nt) {
;                                 acc[x][nt] = __builtin_amdgcn_mfma_f32_16x16x32_bf16(xh, bl[s4][nt], acc[x][nt], 0, 0, 0);
;                                 acc[x][nt] = __builtin_amdgcn_mfma_f32_16x16x32_bf16(xh, bh[s4][nt], acc[x][nt], 0, 0, 0); } }
;                 }
; #pragma unroll
;                 for (int x = 0; x < 2; ++x) {
; #pragma unroll
;                     for (int nt = 0; nt < 3; ++nt)
; #pragma unroll
;                         for (int e = 0; e < 4; ++e) part[(wave * 32 + 16 * x + 4 * kg + e) * 48 + 16 * nt + li] = acc[x][nt][e];
;                     float s1 = ss[x]; s1 += __shfl_xor(s1, 16); s1 += __shfl_xor(s1, 32);
;                     if (kg == 0) ssp[wave * 32 + 16 * x + li] = s1; }
	ds_add_u32 v167, v232 offset:3200
	ds_add_u32 v167, v233 offset:3392
	ds_add_u32 v167, v234 offset:3584
	ds_add_u32 v167, v235 offset:3776
	s_mov_b64 exec, s[12:13]
	ds_add_u32 v168, v236 offset:49216
	s_mov_b64 exec, s[16:17]
	ds_add_u32 v168, v237 offset:49216
	s_mov_b64 exec, s[20:21]
	ds_add_u32 v168, v238 offset:49216
	s_mov_b64 exec, s[22:23]
	ds_add_u32 v168, v239 offset:49216
	s_mov_b64 exec, -1
	v_mfma_f32_16x16x32_bf16 v[224:227], v[92:95], v[180:183], 0
	v_mfma_f32_16x16x32_bf16 v[224:227], v[92:95], v[184:187], v[224:227]
	v_mfma_f32_16x16x32_bf16 v[224:227], v[84:87], v[204:207], v[224:227]
	v_mfma_f32_16x16x32_bf16 v[224:227], v[84:87], v[148:151], v[224:227]
	v_mfma_f32_16x16x32_bf16 v[228:231], v[92:95], v[188:191], 0
	v_mfma_f32_16x16x32_bf16 v[228:231], v[92:95], v[192:195], v[228:231]
	v_mfma_f32_16x16x32_bf16 v[228:231], v[84:87], v[208:211], v[228:231]
	v_mfma_f32_16x16x32_bf16 v[228:231], v[84:87], v[212:215], v[228:231]
	v_mfma_f32_16x16x32_bf16 v[232:235], v[92:95], v[196:199], 0
	v_mfma_f32_16x16x32_bf16 v[232:235], v[92:95], v[200:203], v[232:235]
	v_mfma_f32_16x16x32_bf16 v[232:235], v[84:87], v[216:219], v[232:235]
	v_mfma_f32_16x16x32_bf16 v[232:235], v[84:87], v[220:223], v[232:235]
	v_mfma_f32_16x16x32_bf16 v[236:239], v[92:95], v[92:95], 0
	v_mfma_f32_16x16x32_bf16 v[236:239], v[84:87], v[84:87], v[236:239]
	s_nop 7
	s_nop 3
	v_mul_f32_e32 v224, v224, v176
	v_cvt_i32_f32_e32 v224, v224
	v_mul_f32_e32 v225, v225, v176
	v_cvt_i32_f32_e32 v225, v225
	v_mul_f32_e32 v226, v226, v176
	v_cvt_i32_f32_e32 v226, v226
	v_mul_f32_e32 v227, v227, v176
	v_cvt_i32_f32_e32 v227, v227
	v_mul_f32_e32 v228, v228, v176
	v_cvt_i32_f32_e32 v228, v228
	v_mul_f32_e32 v229, v229, v176
	v_cvt_i32_f32_e32 v229, v229
	v_mul_f32_e32 v230, v230, v176
	v_cvt_i32_f32_e32 v230, v230
	v_mul_f32_e32 v231, v231, v176
	v_cvt_i32_f32_e32 v231, v231
	v_mul_f32_e32 v232, v232, v176
	v_cvt_i32_f32_e32 v232, v232
	v_mul_f32_e32 v233, v233, v176
	v_cvt_i32_f32_e32 v233, v233
	v_mul_f32_e32 v234, v234, v176
	v_cvt_i32_f32_e32 v234, v234
	v_mul_f32_e32 v235, v235, v176
	v_cvt_i32_f32_e32 v235, v235
	v_mul_f32_e32 v236, v236, v177
	v_cvt_i32_f32_e32 v236, v236
	v_mul_f32_e32 v237, v237, v177
	v_cvt_i32_f32_e32 v237, v237
	v_mul_f32_e32 v238, v238, v177
	v_cvt_i32_f32_e32 v238, v238
	v_mul_f32_e32 v239, v239, v177
	v_cvt_i32_f32_e32 v239, v239
	ds_add_u32 v167, v224 offset:6144
	ds_add_u32 v167, v225 offset:6336
	ds_add_u32 v167, v226 offset:6528
	ds_add_u32 v167, v227 offset:6720
	ds_add_u32 v167, v228 offset:6208
	ds_add_u32 v167, v229 offset:6400
	ds_add_u32 v167, v230 offset:6592
	ds_add_u32 v167, v231 offset:6784
	ds_add_u32 v167, v232 offset:6272
	ds_add_u32 v167, v233 offset:6464
	ds_add_u32 v167, v234 offset:6656
	ds_add_u32 v167, v235 offset:6848
	s_mov_b64 exec, s[12:13]
	ds_add_u32 v168, v236 offset:49280
	s_mov_b64 exec, s[16:17]
	ds_add_u32 v168, v237 offset:49280
	s_mov_b64 exec, s[20:21]
	ds_add_u32 v168, v238 offset:49280
	s_mov_b64 exec, s[22:23]
	ds_add_u32 v168, v239 offset:49280
	s_mov_b64 exec, -1
	v_mfma_f32_16x16x32_bf16 v[224:227], v[76:79], v[180:183], 0
	v_mfma_f32_16x16x32_bf16 v[224:227], v[76:79], v[184:187], v[224:227]
	v_mfma_f32_16x16x32_bf16 v[224:227], v[68:71], v[204:207], v[224:227]
	v_mfma_f32_16x16x32_bf16 v[224:227], v[68:71], v[148:151], v[224:227]
	v_mfma_f32_16x16x32_bf16 v[228:231], v[76:79], v[188:191], 0
	v_mfma_f32_16x16x32_bf16 v[228:231], v[76:79], v[192:195], v[228:231]
	v_mfma_f32_16x16x32_bf16 v[228:231], v[68:71], v[208:211], v[228:231]
	v_mfma_f32_16x16x32_bf16 v[228:231], v[68:71], v[212:215], v[228:231]
	v_mfma_f32_16x16x32_bf16 v[232:235], v[76:79], v[196:199], 0
	v_mfma_f32_16x16x32_bf16 v[232:235], v[76:79], v[200:203], v[232:235]
	v_mfma_f32_16x16x32_bf16 v[232:235], v[68:71], v[216:219], v[232:235]
	v_mfma_f32_16x16x32_bf16 v[232:235], v[68:71], v[220:223], v[232:235]
	v_mfma_f32_16x16x32_bf16 v[236:239], v[76:79], v[76:79], 0
	v_mfma_f32_16x16x32_bf16 v[236:239], v[68:71], v[68:71], v[236:239]
	s_nop 7
	s_nop 3
	v_mul_f32_e32 v224, v224, v176
	v_cvt_i32_f32_e32 v224, v224
	v_mul_f32_e32 v225, v225, v176
	v_cvt_i32_f32_e32 v225, v225
	v_mul_f32_e32 v226, v226, v176
	v_cvt_i32_f32_e32 v226, v226
	v_mul_f32_e32 v227, v227, v176
	v_cvt_i32_f32_e32 v227, v227
	v_mul_f32_e32 v228, v228, v176
	v_cvt_i32_f32_e32 v228, v228
	v_mul_f32_e32 v229, v229, v176
	v_cvt_i32_f32_e32 v229, v229
	v_mul_f32_e32 v230, v230, v176
	v_cvt_i32_f32_e32 v230, v230
	v_mul_f32_e32 v231, v231, v176
	v_cvt_i32_f32_e32 v231, v231
	v_mul_f32_e32 v232, v232, v176
	v_cvt_i32_f32_e32 v232, v232
	v_mul_f32_e32 v233, v233, v176
	v_cvt_i32_f32_e32 v233, v233
	v_mul_f32_e32 v234, v234, v176
	v_cvt_i32_f32_e32 v234, v234
	v_mul_f32_e32 v235, v235, v176
	v_cvt_i32_f32_e32 v235, v235
	v_mul_f32_e32 v236, v236, v177
	v_cvt_i32_f32_e32 v236, v236
	v_mul_f32_e32 v237, v237, v177
	v_cvt_i32_f32_e32 v237, v237
	v_mul_f32_e32 v238, v238, v177
	v_cvt_i32_f32_e32 v238, v238
	v_mul_f32_e32 v239, v239, v177
	v_cvt_i32_f32_e32 v239, v239
	ds_add_u32 v167, v224 offset:9216
	ds_add_u32 v167, v225 offset:9408
	ds_add_u32 v167, v226 offset:9600
	ds_add_u32 v167, v227 offset:9792
	ds_add_u32 v167, v228 offset:9280
	ds_add_u32 v167, v229 offset:9472
	ds_add_u32 v167, v230 offset:9664
	ds_add_u32 v167, v231 offset:9856
	ds_add_u32 v167, v232 offset:9344
	ds_add_u32 v167, v233 offset:9536
	ds_add_u32 v167, v234 offset:9728
	ds_add_u32 v167, v235 offset:9920
	s_mov_b64 exec, s[12:13]
	ds_add_u32 v168, v236 offset:49344
	s_mov_b64 exec, s[16:17]
	ds_add_u32 v168, v237 offset:49344
	s_mov_b64 exec, s[20:21]
	ds_add_u32 v168, v238 offset:49344
; __global__ void __launch_bounds__(512, 2) hymba_fwd(Args args) {
;     ...
;                     for (int s4 = 0; s4 < 4; ++s4)
; #pragma unroll
;                         for (int x = 0; x < 2; ++x) { const v4u q = xa[x][s4];
;                             ss[x] += (bf_lo(q.x) * bf_lo(q.x) + bf_hi(q.x) * bf_hi(q.x)) + (bf_lo(q.y) * bf_lo(q.y) + bf_hi(q.y) * bf_hi(q.y)) + (bf_lo(q.z) * bf_lo(q.z) + bf_hi(q.z) * bf_hi(q.z)) + (bf_lo(q.w) * bf_lo(q.w) + bf_hi(q.w) * bf_hi(q.w)); }
;                     __builtin_amdgcn_sched_barrier(0);
; #pragma unroll
;                     for (int s4 = 0; s4 < 4; ++s4)
; #pragma unroll
;                         for (int x = 0; x < 2; ++x) { const bf16x8 xh = __builtin_bit_cast(bf16x8, xa[x][s4]);
; #pragma unroll
;                             for (int nt = 0; nt < 3; ++nt) {
;                                 acc[x][nt] = __builtin_amdgcn_mfma_f32_16x16x32_bf16(xh, bl[s4][nt], acc[x][nt], 0, 0, 0);
;                                 acc[x][nt] = __builtin_amdgcn_mfma_f32_16x16x32_bf16(xh, bh[s4][nt], acc[x][nt], 0, 0, 0); } }
;                 }
; #pragma unroll
;                 for (int x = 0; x < 2; ++x) {
; #pragma unroll
;                     for (int nt = 0; nt < 3; ++nt)
; #pragma unroll
;                         for (int e = 0; e < 4; ++e) part[(wave * 32 + 16 * x + 4 * kg + e) * 48 + 16 * nt + li] = acc[x][nt][e];
;                     float s1 = ss[x]; s1 += __shfl_xor(s1, 16); s1 += __shfl_xor(s1, 32);
;                     if (kg == 0) ssp[wave * 32 + 16 * x + li] = s1; }
	s_mov_b64 exec, s[22:23]
	ds_add_u32 v168, v239 offset:49344
	s_mov_b64 exec, -1
	v_mfma_f32_16x16x32_bf16 v[224:227], v[60:63], v[180:183], 0
	v_mfma_f32_16x16x32_bf16 v[224:227], v[60:63], v[184:187], v[224:227]
	v_mfma_f32_16x16x32_bf16 v[224:227], v[52:55], v[204:207], v[224:227]
	v_mfma_f32_16x16x32_bf16 v[224:227], v[52:55], v[148:151], v[224:227]
	v_mfma_f32_16x16x32_bf16 v[228:231], v[60:63], v[188:191], 0
	v_mfma_f32_16x16x32_bf16 v[228:231], v[60:63], v[192:195], v[228:231]
	v_mfma_f32_16x16x32_bf16 v[228:231], v[52:55], v[208:211], v[228:231]
	v_mfma_f32_16x16x32_bf16 v[228:231], v[52:55], v[212:215], v[228:231]
	v_mfma_f32_16x16x32_bf16 v[232:235], v[60:63], v[196:199], 0
	v_mfma_f32_16x16x32_bf16 v[232:235], v[60:63], v[200:203], v[232:235]
	v_mfma_f32_16x16x32_bf16 v[232:235], v[52:55], v[216:219], v[232:235]
	v_mfma_f32_16x16x32_bf16 v[232:235], v[52:55], v[220:223], v[232:235]
	v_mfma_f32_16x16x32_bf16 v[236:239], v[60:63], v[60:63], 0
	v_mfma_f32_16x16x32_bf16 v[236:239], v[52:55], v[52:55], v[236:239]
	s_nop 7
	s_nop 3
	v_mul_f32_e32 v224, v224, v176
	v_cvt_i32_f32_e32 v224, v224
	v_mul_f32_e32 v225, v225, v176
	v_cvt_i32_f32_e32 v225, v225
	v_mul_f32_e32 v226, v226, v176
	v_cvt_i32_f32_e32 v226, v226
	v_mul_f32_e32 v227, v227, v176
	v_cvt_i32_f32_e32 v227, v227
	v_mul_f32_e32 v228, v228, v176
	v_cvt_i32_f32_e32 v228, v228
	v_mul_f32_e32 v229, v229, v176
	v_cvt_i32_f32_e32 v229, v229
	v_mul_f32_e32 v230, v230, v176
	v_cvt_i32_f32_e32 v230, v230
	v_mul_f32_e32 v231, v231, v176
	v_cvt_i32_f32_e32 v231, v231
	v_mul_f32_e32 v232, v232, v176
	v_cvt_i32_f32_e32 v232, v232
	v_mul_f32_e32 v233, v233, v176
	v_cvt_i32_f32_e32 v233, v233
	v_mul_f32_e32 v234, v234, v176
	v_cvt_i32_f32_e32 v234, v234
	v_mul_f32_e32 v235, v235, v176
	v_cvt_i32_f32_e32 v235, v235
	v_mul_f32_e32 v236, v236, v177
	v_cvt_i32_f32_e32 v236, v236
	v_mul_f32_e32 v237, v237, v177
	v_cvt_i32_f32_e32 v237, v237
	v_mul_f32_e32 v238, v238, v177
	v_cvt_i32_f32_e32 v238, v238
	v_mul_f32_e32 v239, v239, v177
	v_cvt_i32_f32_e32 v239, v239
	ds_add_u32 v167, v224 offset:24576
	ds_add_u32 v167, v225 offset:24768
	ds_add_u32 v167, v226 offset:24960
	ds_add_u32 v167, v227 offset:25152
	ds_add_u32 v167, v228 offset:24640
	ds_add_u32 v167, v229 offset:24832
	ds_add_u32 v167, v230 offset:25024
	ds_add_u32 v167, v231 offset:25216
	ds_add_u32 v167, v232 offset:24704
	ds_add_u32 v167, v233 offset:24896
	ds_add_u32 v167, v234 offset:25088
	ds_add_u32 v167, v235 offset:25280
	s_mov_b64 exec, s[12:13]
	ds_add_u32 v168, v236 offset:49664
	s_mov_b64 exec, s[16:17]
	ds_add_u32 v168, v237 offset:49664
	s_mov_b64 exec, s[20:21]
	ds_add_u32 v168, v238 offset:49664
	s_mov_b64 exec, s[22:23]
	ds_add_u32 v168, v239 offset:49664
	s_mov_b64 exec, -1
	v_mfma_f32_16x16x32_bf16 v[224:227], v[44:47], v[180:183], 0
	v_mfma_f32_16x16x32_bf16 v[224:227], v[44:47], v[184:187], v[224:227]
	v_mfma_f32_16x16x32_bf16 v[224:227], v[36:39], v[204:207], v[224:227]
	v_mfma_f32_16x16x32_bf16 v[224:227], v[36:39], v[148:151], v[224:227]
	v_mfma_f32_16x16x32_bf16 v[228:231], v[44:47], v[188:191], 0
	v_mfma_f32_16x16x32_bf16 v[228:231], v[44:47], v[192:195], v[228:231]
	v_mfma_f32_16x16x32_bf16 v[228:231], v[36:39], v[208:211], v[228:231]
	v_mfma_f32_16x16x32_bf16 v[228:231], v[36:39], v[212:215], v[228:231]
	v_mfma_f32_16x16x32_bf16 v[232:235], v[44:47], v[196:199], 0
	v_mfma_f32_16x16x32_bf16 v[232:235], v[44:47], v[200:203], v[232:235]
	v_mfma_f32_16x16x32_bf16 v[232:235], v[36:39], v[216:219], v[232:235]
	v_mfma_f32_16x16x32_bf16 v[232:235], v[36:39], v[220:223], v[232:235]
	v_mfma_f32_16x16x32_bf16 v[236:239], v[44:47], v[44:47], 0
	v_mfma_f32_16x16x32_bf16 v[236:239], v[36:39], v[36:39], v[236:239]
	s_nop 7
	s_nop 3
	v_mul_f32_e32 v224, v224, v176
	v_cvt_i32_f32_e32 v224, v224
	v_mul_f32_e32 v225, v225, v176
	v_cvt_i32_f32_e32 v225, v225
	v_mul_f32_e32 v226, v226, v176
	v_cvt_i32_f32_e32 v226, v226
	v_mul_f32_e32 v227, v227, v176
	v_cvt_i32_f32_e32 v227, v227
	v_mul_f32_e32 v228, v228, v176
	v_cvt_i32_f32_e32 v228, v228
	v_mul_f32_e32 v229, v229, v176
	v_cvt_i32_f32_e32 v229, v229
	v_mul_f32_e32 v230, v230, v176
	v_cvt_i32_f32_e32 v230, v230
	v_mul_f32_e32 v231, v231, v176
	v_cvt_i32_f32_e32 v231, v231
	v_mul_f32_e32 v232, v232, v176
	v_cvt_i32_f32_e32 v232, v232
	v_mul_f32_e32 v233, v233, v176
	v_cvt_i32_f32_e32 v233, v233
	v_mul_f32_e32 v234, v234, v176
	v_cvt_i32_f32_e32 v234, v234
	v_mul_f32_e32 v235, v235, v176
	v_cvt_i32_f32_e32 v235, v235
	v_mul_f32_e32 v236, v236, v177
	v_cvt_i32_f32_e32 v236, v236
	v_mul_f32_e32 v237, v237, v177
	v_cvt_i32_f32_e32 v237, v237
	v_mul_f32_e32 v238, v238, v177
	v_cvt_i32_f32_e32 v238, v238
	v_mul_f32_e32 v239, v239, v177
	v_cvt_i32_f32_e32 v239, v239
	ds_add_u32 v167, v224 offset:27648
	ds_add_u32 v167, v225 offset:27840
	ds_add_u32 v167, v226 offset:28032
	ds_add_u32 v167, v227 offset:28224
	ds_add_u32 v167, v228 offset:27712
	ds_add_u32 v167, v229 offset:27904
	ds_add_u32 v167, v230 offset:28096
	ds_add_u32 v167, v231 offset:28288
	ds_add_u32 v167, v232 offset:27776
	ds_add_u32 v167, v233 offset:27968
	ds_add_u32 v167, v234 offset:28160
	ds_add_u32 v167, v235 offset:28352
	s_mov_b64 exec, s[12:13]
	ds_add_u32 v168, v236 offset:49728
	s_mov_b64 exec, s[16:17]
	ds_add_u32 v168, v237 offset:49728
	s_mov_b64 exec, s[20:21]
	ds_add_u32 v168, v238 offset:49728
	s_mov_b64 exec, s[22:23]
	ds_add_u32 v168, v239 offset:49728
	s_mov_b64 exec, -1
	v_mfma_f32_16x16x32_bf16 v[224:227], v[20:23], v[180:183], 0
	v_mfma_f32_16x16x32_bf16 v[224:227], v[20:23], v[184:187], v[224:227]
	v_mfma_f32_16x16x32_bf16 v[224:227], v[24:27], v[204:207], v[224:227]
; __global__ void __launch_bounds__(512, 2) hymba_fwd(Args args) {
;     ...
; #pragma unroll
;                 for (int x = 0; x < 2; ++x) {
; #pragma unroll
;                     for (int nt = 0; nt < 3; ++nt)
; #pragma unroll
;                         for (int e = 0; e < 4; ++e) part[(wave * 32 + 16 * x + 4 * kg + e) * 48 + 16 * nt + li] = acc[x][nt][e];
;                     float s1 = ss[x]; s1 += __shfl_xor(s1, 16); s1 += __shfl_xor(s1, 32);
;                     if (kg == 0) ssp[wave * 32 + 16 * x + li] = s1; }
;             }
;             __syncthreads();
;             for (int idx = tid; idx < 32 * 48; idx += 512) { float a = 0.f;
; #pragma unroll
;                 for (int w8 = 0; w8 < 8; ++w8) a += part[w8 * 1536 + idx];
;                 logit[idx] = a; }
;             if (tid < 32) { float a = 0.f;
; #pragma unroll
;                 for (int w8 = 0; w8 < 8; ++w8) a += ssp[w8 * 32 + tid];
;                 const float r = __builtin_amdgcn_rsqf(a * (1.f / DM) + NORM_EPS); rsl[tid] = r; rstd_g[t0 + tid] = r; }
	v_mfma_f32_16x16x32_bf16 v[224:227], v[24:27], v[148:151], v[224:227]
	v_mfma_f32_16x16x32_bf16 v[228:231], v[20:23], v[188:191], 0
	v_mfma_f32_16x16x32_bf16 v[228:231], v[20:23], v[192:195], v[228:231]
	v_mfma_f32_16x16x32_bf16 v[228:231], v[24:27], v[208:211], v[228:231]
	v_mfma_f32_16x16x32_bf16 v[228:231], v[24:27], v[212:215], v[228:231]
	v_mfma_f32_16x16x32_bf16 v[232:235], v[20:23], v[196:199], 0
	v_mfma_f32_16x16x32_bf16 v[232:235], v[20:23], v[200:203], v[232:235]
	v_mfma_f32_16x16x32_bf16 v[232:235], v[24:27], v[216:219], v[232:235]
	v_mfma_f32_16x16x32_bf16 v[232:235], v[24:27], v[220:223], v[232:235]
	v_mfma_f32_16x16x32_bf16 v[236:239], v[20:23], v[20:23], 0
	v_mfma_f32_16x16x32_bf16 v[236:239], v[24:27], v[24:27], v[236:239]
	s_nop 7
	s_nop 3
	v_mul_f32_e32 v224, v224, v176
	v_cvt_i32_f32_e32 v224, v224
	v_mul_f32_e32 v225, v225, v176
	v_cvt_i32_f32_e32 v225, v225
	v_mul_f32_e32 v226, v226, v176
	v_cvt_i32_f32_e32 v226, v226
	v_mul_f32_e32 v227, v227, v176
	v_cvt_i32_f32_e32 v227, v227
	v_mul_f32_e32 v228, v228, v176
	v_cvt_i32_f32_e32 v228, v228
	v_mul_f32_e32 v229, v229, v176
	v_cvt_i32_f32_e32 v229, v229
	v_mul_f32_e32 v230, v230, v176
	v_cvt_i32_f32_e32 v230, v230
	v_mul_f32_e32 v231, v231, v176
	v_cvt_i32_f32_e32 v231, v231
	v_mul_f32_e32 v232, v232, v176
	v_cvt_i32_f32_e32 v232, v232
	v_mul_f32_e32 v233, v233, v176
	v_cvt_i32_f32_e32 v233, v233
	v_mul_f32_e32 v234, v234, v176
	v_cvt_i32_f32_e32 v234, v234
	v_mul_f32_e32 v235, v235, v176
	v_cvt_i32_f32_e32 v235, v235
	v_mul_f32_e32 v236, v236, v177
	v_cvt_i32_f32_e32 v236, v236
	v_mul_f32_e32 v237, v237, v177
	v_cvt_i32_f32_e32 v237, v237
	v_mul_f32_e32 v238, v238, v177
	v_cvt_i32_f32_e32 v238, v238
	v_mul_f32_e32 v239, v239, v177
	v_cvt_i32_f32_e32 v239, v239
	ds_add_u32 v167, v224 offset:30720
	ds_add_u32 v167, v225 offset:30912
	ds_add_u32 v167, v226 offset:31104
	ds_add_u32 v167, v227 offset:31296
	ds_add_u32 v167, v228 offset:30784
	ds_add_u32 v167, v229 offset:30976
	ds_add_u32 v167, v230 offset:31168
	ds_add_u32 v167, v231 offset:31360
	ds_add_u32 v167, v232 offset:30848
	ds_add_u32 v167, v233 offset:31040
	ds_add_u32 v167, v234 offset:31232
	ds_add_u32 v167, v235 offset:31424
	s_mov_b64 exec, s[12:13]
	ds_add_u32 v168, v236 offset:49792
	s_mov_b64 exec, s[16:17]
	ds_add_u32 v168, v237 offset:49792
	s_mov_b64 exec, s[20:21]
	ds_add_u32 v168, v238 offset:49792
	s_mov_b64 exec, s[22:23]
	ds_add_u32 v168, v239 offset:49792
	s_mov_b64 exec, -1
	v_mfma_f32_16x16x32_bf16 v[224:227], v[4:7], v[180:183], 0
	v_mfma_f32_16x16x32_bf16 v[224:227], v[4:7], v[184:187], v[224:227]
	v_mfma_f32_16x16x32_bf16 v[224:227], v[8:11], v[204:207], v[224:227]
	v_mfma_f32_16x16x32_bf16 v[224:227], v[8:11], v[148:151], v[224:227]
	v_mfma_f32_16x16x32_bf16 v[228:231], v[4:7], v[188:191], 0
	v_mfma_f32_16x16x32_bf16 v[228:231], v[4:7], v[192:195], v[228:231]
	v_mfma_f32_16x16x32_bf16 v[228:231], v[8:11], v[208:211], v[228:231]
	v_mfma_f32_16x16x32_bf16 v[228:231], v[8:11], v[212:215], v[228:231]
	v_mfma_f32_16x16x32_bf16 v[232:235], v[4:7], v[196:199], 0
	v_mfma_f32_16x16x32_bf16 v[232:235], v[4:7], v[200:203], v[232:235]
	v_mfma_f32_16x16x32_bf16 v[232:235], v[8:11], v[216:219], v[232:235]
	v_mfma_f32_16x16x32_bf16 v[232:235], v[8:11], v[220:223], v[232:235]
	v_mfma_f32_16x16x32_bf16 v[236:239], v[4:7], v[4:7], 0
	v_mfma_f32_16x16x32_bf16 v[236:239], v[8:11], v[8:11], v[236:239]
	s_nop 7
	s_nop 3
	v_mul_f32_e32 v224, v224, v176
	v_cvt_i32_f32_e32 v224, v224
	v_mul_f32_e32 v225, v225, v176
	v_cvt_i32_f32_e32 v225, v225
	v_mul_f32_e32 v226, v226, v176
	v_cvt_i32_f32_e32 v226, v226
	v_mul_f32_e32 v227, v227, v176
	v_cvt_i32_f32_e32 v227, v227
	v_mul_f32_e32 v228, v228, v176
	v_cvt_i32_f32_e32 v228, v228
	v_mul_f32_e32 v229, v229, v176
	v_cvt_i32_f32_e32 v229, v229
	v_mul_f32_e32 v230, v230, v176
	v_cvt_i32_f32_e32 v230, v230
	v_mul_f32_e32 v231, v231, v176
	v_cvt_i32_f32_e32 v231, v231
	v_mul_f32_e32 v232, v232, v176
	v_cvt_i32_f32_e32 v232, v232
	v_mul_f32_e32 v233, v233, v176
	v_cvt_i32_f32_e32 v233, v233
	v_mul_f32_e32 v234, v234, v176
	v_cvt_i32_f32_e32 v234, v234
	v_mul_f32_e32 v235, v235, v176
	v_cvt_i32_f32_e32 v235, v235
	v_mul_f32_e32 v236, v236, v177
	v_cvt_i32_f32_e32 v236, v236
	v_mul_f32_e32 v237, v237, v177
	v_cvt_i32_f32_e32 v237, v237
	v_mul_f32_e32 v238, v238, v177
	v_cvt_i32_f32_e32 v238, v238
	v_mul_f32_e32 v239, v239, v177
	v_cvt_i32_f32_e32 v239, v239
	ds_add_u32 v167, v224 offset:33792
	ds_add_u32 v167, v225 offset:33984
	ds_add_u32 v167, v226 offset:34176
	ds_add_u32 v167, v227 offset:34368
	ds_add_u32 v167, v228 offset:33856
	ds_add_u32 v167, v229 offset:34048
	ds_add_u32 v167, v230 offset:34240
	ds_add_u32 v167, v231 offset:34432
	ds_add_u32 v167, v232 offset:33920
	ds_add_u32 v167, v233 offset:34112
	ds_add_u32 v167, v234 offset:34304
	ds_add_u32 v167, v235 offset:34496
	s_mov_b64 exec, s[12:13]
	ds_add_u32 v168, v236 offset:49856
	s_mov_b64 exec, s[16:17]
	ds_add_u32 v168, v237 offset:49856
	s_mov_b64 exec, s[20:21]
	ds_add_u32 v168, v238 offset:49856
	s_mov_b64 exec, s[22:23]
	ds_add_u32 v168, v239 offset:49856
	s_mov_b64 exec, -1
	s_waitcnt lgkmcnt(0)
	s_barrier
	ds_read_b128 v[180:183], v170 offset:0
	ds_read_b128 v[184:187], v170 offset:1024
	ds_read_b128 v[188:191], v170 offset:2048
	ds_read_b128 v[192:195], v170 offset:3072
	ds_read_b128 v[196:199], v170 offset:4096
	ds_read_b128 v[200:203], v170 offset:5120
	ds_read_b32 v204, v171 offset:49152
	s_lshl_b32 s33, s84, 13
	s_lshl_b32 s41, s48, 8
	s_add_i32 s33, s33, s41
	s_lshl_b32 s41, s100, 5
	s_add_i32 s33, s33, s41
	s_mul_i32 s41, s33, 0xc0
	s_add_u32 s12, s26, 0x15000000
	s_addc_u32 s13, s27, 0
	s_add_u32 s12, s12, s41
	s_addc_u32 s13, s13, 0
	v_lshlrev_b32_e32 v205, 4, v164
	s_waitcnt lgkmcnt(0)
	global_store_dwordx4 v205, v[180:183], s[12:13] sc0 sc1
	global_store_dwordx4 v205, v[184:187], s[12:13] offset:1024 sc0 sc1
	global_store_dwordx4 v205, v[188:191], s[12:13] offset:2048 sc0 sc1
	global_store_dwordx4 v205, v[192:195], s[12:13] offset:3072 sc0 sc1
	s_add_u32 s12, s12, 0x1000
	s_addc_u32 s13, s13, 0
	global_store_dwordx4 v205, v[196:199], s[12:13] sc0 sc1
	global_store_dwordx4 v205, v[200:203], s[12:13] offset:1024 sc0 sc1
	s_lshl_b32 s41, s33, 2
	s_add_u32 s12, s26, 0x16000000
	s_addc_u32 s13, s27, 0
	s_add_u32 s12, s12, s41
	s_addc_u32 s13, s13, 0
	v_lshlrev_b32_e32 v205, 2, v164
	s_mov_b32 exec_lo, -1
	s_mov_b32 exec_hi, 0
	global_store_dword v205, v204, s[12:13] sc0 sc1
	s_mov_b64 exec, -1
	v_mov_b64_e32 v[144:145], 0x100
	v_mov_b64_e32 v[146:147], 0xff
	s_waitcnt vmcnt(0)
	s_barrier
	s_lshl_b32 s41, s48, 6
	s_add_i32 s41, s41, 0x6000
	s_add_u32 s12, s26, s41
	s_addc_u32 s13, s27, 0
	v_mov_b32_e32 v204, 1
	v_mov_b32_e32 v205, 0
	s_cmp_lg_u32 s100, 0
	s_cbranch_scc1 .Lms_nopub
	s_mov_b64 exec, 1
	global_atomic_add v205, v204, s[12:13]
	s_mov_b64 exec, -1
.Lms_nopub:
	s_andn2_b64 vcc, exec, s[0:1]
	s_mov_b64 s[0:1], -1
	s_cbranch_vccnz .LBB0_478
	s_andn2_b64 vcc, exec, s[4:5]
	s_cbranch_vccnz .LBB0_477
	s_barrier
	s_branch .LBB0_477

; __device__ __forceinline__ unsigned xb_add(unsigned* p, unsigned v) { return __hip_atomic_fetch_add(p, v, __ATOMIC_RELAXED, __HIP_MEMORY_SCOPE_AGENT); }
; __device__ __forceinline__ void xcd_barrier(const XcdBarrier& b, const int tid) {
;     asm volatile("s_waitcnt vmcnt(0)" ::: "memory");
;     __syncthreads();
;     if (tid == 0) {
;         unsigned* bar = b.bar;
;         __builtin_amdgcn_s_waitcnt(0);
;         unsigned nloc = b.st[0], nx = b.st[1];
;         if (nloc == 0u) { xcd_barrier_complete(bar, b.x, nloc, nx); b.st[0] = nloc; b.st[1] = nx; }
;         const unsigned old = xb_add(&bar[XB_XSUB(b.x)], 1u);
;         const unsigned gen = old / nloc;
;         if (old + 1u == (gen + 1u) * nloc) {
.LBB0_493:
	s_branch .LBB0_547
	v_mbcnt_lo_u32_b32 v0, -1, 0
	v_mbcnt_hi_u32_b32 v0, -1, v0
	s_waitcnt vmcnt(0)
	s_nop 0
	v_sub_u32_e32 v0, 0, v0
	v_cmp_eq_u32_e32 vcc, s93, v0
	s_barrier
	s_and_saveexec_b64 s[0:1], vcc
	s_cbranch_execz .LBB0_546
	s_add_i32 s4, 0, 0x22600
	v_mov_b32_e32 v0, s4
	s_waitcnt vmcnt(0) expcnt(0) lgkmcnt(0)
	ds_read_b32 v2, v0
	s_add_i32 s4, 0, 0x22604
	v_mov_b32_e32 v0, s4
	ds_read_b32 v0, v0
	s_waitcnt lgkmcnt(1)
	v_cmp_ne_u32_e32 vcc, 0, v2
	s_cbranch_vccnz .LBB0_510
	v_readlane_b32 s4, v255, 0
	v_readlane_b32 s5, v255, 1
	s_load_dwordx2 s[8:9], s[4:5], 0x4
	s_add_u32 s4, s26, 0x1000
	s_addc_u32 s5, s27, 0
	s_add_u32 s6, s26, 0x1100
	s_addc_u32 s7, s27, 0
	s_waitcnt lgkmcnt(0)
	s_mul_i32 s22, s8, s3
	s_add_u32 s8, s26, 0x1200
	s_mul_i32 s22, s22, s9
	s_addc_u32 s9, s27, 0
	s_add_u32 s10, s26, 0x1300
	s_addc_u32 s11, s27, 0
	s_mov_b32 s23, 1
	v_mov_b32_e32 v16, 0
	s_branch .LBB0_498

; __global__ void __launch_bounds__(512, 2) hymba_fwd(Args args) {
;     ...
;             __syncthreads();
;             for (int idx = tid; idx < 32 * 48; idx += 512) { float a = 0.f;
; #pragma unroll
;                 for (int w8 = 0; w8 < 8; ++w8) a += part[w8 * 1536 + idx];
;                 logit[idx] = a; }
;             if (tid < 32) { float a = 0.f;
; #pragma unroll
;                 for (int w8 = 0; w8 < 8; ++w8) a += ssp[w8 * 32 + tid];
;                 const float r = __builtin_amdgcn_rsqf(a * (1.f / DM) + NORM_EPS); rsl[tid] = r; rstd_g[t0 + tid] = r; }
.LBB0_553:
	s_lshl_b32 s33, s66, 5
	s_lshr_b32 s16, s66, 3
	s_lshl_b32 s16, s16, 6
	s_add_i32 s16, s16, 0x6000
	s_add_u32 s20, s26, s16
	s_addc_u32 s21, s27, 0
	v_mov_b32_e32 v0, 0
	s_mov_b32 s16, 0
.Lms_spin:
	global_load_dword v1, v0, s[20:21] sc0 sc1
	s_waitcnt vmcnt(0)
	v_readfirstlane_b32 s17, v1
	s_cmp_ge_u32 s17, 8
	s_cbranch_scc1 .Lms_done
	s_sleep 2
	s_add_i32 s16, s16, 1
	s_cmpk_lt_u32 s16, 0x400
	s_cbranch_scc1 .Lms_spin
.Lms_done:
	s_lshl_b32 s16, s92, 13
	s_add_i32 s16, s16, s33
	s_mul_i32 s17, s16, 0xc0
	s_add_u32 s20, s26, 0x15000000
	s_addc_u32 s21, s27, 0
	s_add_u32 s20, s20, s17
	s_addc_u32 s21, s21, 0
	v_mbcnt_lo_u32_b32 v0, -1, 0
	v_mbcnt_hi_u32_b32 v0, -1, v0
	v_lshlrev_b32_e32 v1, 4, v0
	global_load_dwordx4 v[8:11], v1, s[20:21] sc0 sc1
	global_load_dwordx4 v[12:15], v1, s[20:21] offset:1024 sc0 sc1
	global_load_dwordx4 v[16:19], v1, s[20:21] offset:2048 sc0 sc1
	global_load_dwordx4 v[20:23], v1, s[20:21] offset:3072 sc0 sc1
	s_add_u32 s20, s20, 0x1000
	s_addc_u32 s21, s21, 0
	global_load_dwordx4 v[24:27], v1, s[20:21] sc0 sc1
	global_load_dwordx4 v[28:31], v1, s[20:21] offset:1024 sc0 sc1
	s_lshl_b32 s17, s16, 2
	s_add_u32 s20, s26, 0x16000000
	s_addc_u32 s21, s27, 0
	s_add_u32 s20, s20, s17
	s_addc_u32 s21, s21, 0
	v_lshlrev_b32_e32 v2, 2, v0
	global_load_dword v3, v2, s[20:21] sc0 sc1
	s_mul_i32 s17, s92, 0x1800
	v_add_u32_e32 v4, s17, v1
	s_lshl_b32 s17, s92, 7
	v_add_u32_e32 v5, s17, v2
	v_mov_b32_e32 v6, 0x33800000
	v_mov_b32_e32 v7, 0x37800000
	s_waitcnt vmcnt(0)
	v_cvt_f32_i32_e32 v8, v8
	v_cvt_f32_i32_e32 v9, v9
	v_cvt_f32_i32_e32 v10, v10
	v_cvt_f32_i32_e32 v11, v11
	v_cvt_f32_i32_e32 v12, v12
	v_cvt_f32_i32_e32 v13, v13
	v_cvt_f32_i32_e32 v14, v14
	v_cvt_f32_i32_e32 v15, v15
	v_cvt_f32_i32_e32 v16, v16
	v_cvt_f32_i32_e32 v17, v17
	v_cvt_f32_i32_e32 v18, v18
	v_cvt_f32_i32_e32 v19, v19
	v_cvt_f32_i32_e32 v20, v20
	v_cvt_f32_i32_e32 v21, v21
	v_cvt_f32_i32_e32 v22, v22
	v_cvt_f32_i32_e32 v23, v23
	v_cvt_f32_i32_e32 v24, v24
	v_cvt_f32_i32_e32 v25, v25
	v_cvt_f32_i32_e32 v26, v26
	v_cvt_f32_i32_e32 v27, v27
	v_cvt_f32_i32_e32 v28, v28
	v_cvt_f32_i32_e32 v29, v29
	v_cvt_f32_i32_e32 v30, v30
	v_cvt_f32_i32_e32 v31, v31
	v_mul_f32_e32 v8, v8, v6
	v_mul_f32_e32 v9, v9, v6
	v_mul_f32_e32 v10, v10, v6
	v_mul_f32_e32 v11, v11, v6
	v_mul_f32_e32 v12, v12, v6
	v_mul_f32_e32 v13, v13, v6
	v_mul_f32_e32 v14, v14, v6
	v_mul_f32_e32 v15, v15, v6
	v_mul_f32_e32 v16, v16, v6
	v_mul_f32_e32 v17, v17, v6
	v_mul_f32_e32 v18, v18, v6
	v_mul_f32_e32 v19, v19, v6
	v_mul_f32_e32 v20, v20, v6
	v_mul_f32_e32 v21, v21, v6
	v_mul_f32_e32 v22, v22, v6
	v_mul_f32_e32 v23, v23, v6
	v_mul_f32_e32 v24, v24, v6
	v_mul_f32_e32 v25, v25, v6
	v_mul_f32_e32 v26, v26, v6
	v_mul_f32_e32 v27, v27, v6
	v_mul_f32_e32 v28, v28, v6
	v_mul_f32_e32 v29, v29, v6
	v_mul_f32_e32 v30, v30, v6
	v_mul_f32_e32 v31, v31, v6
	v_cvt_f32_i32_e32 v3, v3
	s_nop 0
	v_mul_f32_e32 v3, v3, v7
	ds_write_b128 v4, v[8:11]
	ds_write_b128 v4, v[12:15] offset:1024
	ds_write_b128 v4, v[16:19] offset:2048
	ds_write_b128 v4, v[20:23] offset:3072
	ds_write_b128 v4, v[24:27] offset:4096
	ds_write_b128 v4, v[28:31] offset:5120
	s_mov_b32 exec_lo, -1
	s_mov_b32 exec_hi, 0
	ds_write_b32 v5, v3 offset:55296
	s_mov_b64 exec, -1
	s_waitcnt lgkmcnt(0)
	s_barrier
	s_and_saveexec_b64 s[12:13], s[14:15]
	s_cbranch_execz .LBB0_572
	s_mov_b64 s[20:21], -1
	v_mov_b32_e32 v1, v152
	s_and_saveexec_b64 s[16:17], s[18:19]
	s_cbranch_execz .LBB0_569
	v_mov_b32_e32 v2, 0
	s_and_saveexec_b64 s[20:21], s[6:7]
	s_cbranch_execz .LBB0_565
	s_mov_b32 s42, 0
	s_mov_b64 s[46:47], 0
	v_mov_b32_e32 v0, v179
	v_mov_b32_e32 v1, v176
